# MoBA tile loops: tile(i+2) LDS-DMA pair issued inside the QK^T MFMA chain (after the 4th MFMA)
# speedup vs baseline: 1.0008x; 1.0008x over previous
.LBB0_493:
	s_andn2_b64 vcc, exec, s[6:7]
	s_andn2_b64 s[6:7], s[44:45], exec
	s_and_b64 s[46:47], s[44:45], exec
	s_or_b64 s[46:47], s[6:7], s[46:47]
	s_cbranch_vccnz .LBB0_485
	v_add_u32_e32 v32, s56, v199
	v_cvt_f32_i32_e32 v32, v32
	v_add_u32_e32 v160, s33, v165
	s_lshl_b32 s6, 1, s52
	ds_read_b128 v[80:83], v160
	ds_read_b128 v[84:87], v160 offset:512
	ds_read_b128 v[88:91], v160 offset:2048
	ds_read_b128 v[96:99], v160 offset:2560
	v_and_b32_e32 v33, s6, v198
	v_cmp_ne_u32_e32 vcc, 0, v33
	v_fma_f32 v32, v137, v32, -v197
	s_or_b64 vcc, s[0:1], vcc
	v_cndmask_b32_e32 v32, v192, v32, vcc
	v_pk_add_f32 v[48:49], v[136:137], v[32:33] op_sel_hi:[1,0]
	v_pk_add_f32 v[50:51], v[142:143], v[32:33] op_sel_hi:[1,0]
	v_pk_add_f32 v[52:53], v[144:145], v[32:33] op_sel_hi:[1,0]
	v_pk_add_f32 v[54:55], v[146:147], v[32:33] op_sel_hi:[1,0]
	v_pk_add_f32 v[56:57], v[148:149], v[32:33] op_sel_hi:[1,0]
	v_pk_add_f32 v[58:59], v[150:151], v[32:33] op_sel_hi:[1,0]
	v_pk_add_f32 v[60:61], v[152:153], v[32:33] op_sel_hi:[1,0]
	v_pk_add_f32 v[62:63], v[154:155], v[32:33] op_sel_hi:[1,0]
	v_mov_b32_e32 v139, v138
	v_pk_add_f32 v[46:47], v[138:139], v[62:63]
	v_pk_add_f32 v[44:45], v[138:139], v[60:61]
	v_pk_add_f32 v[42:43], v[138:139], v[58:59]
	v_pk_add_f32 v[40:41], v[138:139], v[56:57]
	v_pk_add_f32 v[38:39], v[138:139], v[54:55]
	v_pk_add_f32 v[36:37], v[138:139], v[52:53]
	v_pk_add_f32 v[34:35], v[138:139], v[50:51]
	v_pk_add_f32 v[32:33], v[140:141], v[48:49]
	v_add_u32_e32 v139, s33, v166
	ds_read_b64_tr_b16 v[100:101], v139 offset:24576
	ds_read_b64_tr_b16 v[102:103], v139 offset:25088
	ds_read_b64_tr_b16 v[92:93], v139 offset:25600
	ds_read_b64_tr_b16 v[94:95], v139 offset:26112
	ds_read_b128 v[104:107], v160 offset:4096
	ds_read_b128 v[108:111], v160 offset:4608
	s_waitcnt lgkmcnt(0)
	v_mfma_f32_32x32x16_bf16 v[48:63], v[80:83], v[76:79], v[48:63]
	v_mfma_f32_32x32x16_bf16 v[32:47], v[84:87], v[76:79], v[32:47]
	ds_read_b64_tr_b16 v[84:85], v139 offset:26624
	ds_read_b64_tr_b16 v[86:87], v139 offset:27136
	ds_read_b64_tr_b16 v[80:81], v139 offset:27648
	ds_read_b64_tr_b16 v[82:83], v139 offset:28160
	ds_read_b128 v[202:205], v160 offset:6144
	ds_read_b128 v[206:209], v160 offset:6656
	v_mfma_f32_32x32x16_bf16 v[48:63], v[88:91], v[72:75], v[48:63]
	v_mfma_f32_32x32x16_bf16 v[32:47], v[96:99], v[72:75], v[32:47]
	s_add_i32 s32, s51, 2
	s_cmp_ge_u32 s32, s57
	s_cbranch_scc1 .Lmoba0_a
	s_add_i32 s32, s18, s50
	s_mov_b32 m0, s32
	s_nop 0
	global_load_lds_dwordx4 v[156:157], off
	s_add_i32 m0, s32, 0x6000
	s_nop 0
	global_load_lds_dwordx4 v[158:159], off
.Lmoba0_a:
	v_mfma_f32_32x32x16_bf16 v[48:63], v[104:107], v[68:71], v[48:63]
	v_mfma_f32_32x32x16_bf16 v[32:47], v[108:111], v[68:71], v[32:47]
	s_waitcnt lgkmcnt(0)
	v_mfma_f32_32x32x16_bf16 v[48:63], v[202:205], v[64:67], v[48:63]
	ds_read_b64_tr_b16 v[108:109], v139 offset:28672
	ds_read_b64_tr_b16 v[110:111], v139 offset:29184
	ds_read_b64_tr_b16 v[104:105], v139 offset:29696
	ds_read_b64_tr_b16 v[106:107], v139 offset:30208
	v_mfma_f32_32x32x16_bf16 v[32:47], v[206:209], v[64:67], v[32:47]
	ds_read_b64_tr_b16 v[96:97], v139 offset:30720
	ds_read_b64_tr_b16 v[98:99], v139 offset:31232
	ds_read_b64_tr_b16 v[88:89], v139 offset:31744
	ds_read_b64_tr_b16 v[90:91], v139 offset:32256
	s_add_i32 s6, s56, 63
	s_cmp_gt_u32 s6, s8
	s_cselect_b64 s[6:7], -1, 0
	s_and_b64 s[0:1], s[0:1], s[6:7]
	s_andn2_b64 vcc, exec, s[0:1]
	s_cbranch_vccnz .LBB0_496
	v_add_u32_e32 v139, 27, v200
	v_cmp_lt_i32_e32 vcc, -1, v139
	s_nop 1
	v_cndmask_b32_e32 v48, v192, v48, vcc
	v_cmp_lt_i32_e32 vcc, 31, v139
	v_add_u32_e32 v139, 26, v200
	s_nop 0
	v_cndmask_b32_e32 v32, v192, v32, vcc
	v_cmp_lt_i32_e32 vcc, -1, v139
	s_nop 1
	v_cndmask_b32_e32 v49, v192, v49, vcc
	v_cmp_lt_i32_e32 vcc, 31, v139
	v_add_u32_e32 v139, 25, v200
	s_nop 0
	v_cndmask_b32_e32 v33, v192, v33, vcc
	v_cmp_lt_i32_e32 vcc, -1, v139
	s_nop 1
	v_cndmask_b32_e32 v50, v192, v50, vcc
	v_cmp_lt_i32_e32 vcc, 31, v139
	v_add_u32_e32 v139, 24, v200
	s_nop 0
	v_cndmask_b32_e32 v34, v192, v34, vcc
	v_cmp_lt_i32_e32 vcc, -1, v139
	s_nop 1
	v_cndmask_b32_e32 v51, v192, v51, vcc
	v_cmp_lt_i32_e32 vcc, 31, v139
	v_add_u32_e32 v139, 19, v200
	s_nop 0
	v_cndmask_b32_e32 v35, v192, v35, vcc
	v_cmp_lt_i32_e32 vcc, -1, v139
	s_nop 1
	v_cndmask_b32_e32 v52, v192, v52, vcc
	v_cmp_lt_i32_e32 vcc, 31, v139
	v_add_u32_e32 v139, 18, v200
	s_nop 0
	v_cndmask_b32_e32 v36, v192, v36, vcc
	v_cmp_lt_i32_e32 vcc, -1, v139
	s_nop 1
	v_cndmask_b32_e32 v53, v192, v53, vcc
	v_cmp_lt_i32_e32 vcc, 31, v139
	v_add_u32_e32 v139, 17, v200
	s_nop 0
	v_cndmask_b32_e32 v37, v192, v37, vcc
	v_cmp_lt_i32_e32 vcc, -1, v139
	s_nop 1
	v_cndmask_b32_e32 v54, v192, v54, vcc
	v_cmp_lt_i32_e32 vcc, 31, v139
	v_add_u32_e32 v139, 16, v200
	s_nop 0
	v_cndmask_b32_e32 v38, v192, v38, vcc
	v_cmp_lt_i32_e32 vcc, -1, v139
	s_nop 1
	v_cndmask_b32_e32 v55, v192, v55, vcc
	v_cmp_lt_i32_e32 vcc, 31, v139
	v_add_u32_e32 v139, 11, v200
	s_nop 0
	v_cndmask_b32_e32 v39, v192, v39, vcc
	v_cmp_lt_i32_e32 vcc, -1, v139
	s_nop 1
	v_cndmask_b32_e32 v56, v192, v56, vcc
	v_cmp_lt_i32_e32 vcc, 31, v139
	v_add_u32_e32 v139, 10, v200
	s_nop 0
	v_cndmask_b32_e32 v40, v192, v40, vcc
	v_cmp_lt_i32_e32 vcc, -1, v139
	s_nop 1
	v_cndmask_b32_e32 v57, v192, v57, vcc
	v_cmp_lt_i32_e32 vcc, 31, v139
	v_add_u32_e32 v139, 9, v200
	s_nop 0
	v_cndmask_b32_e32 v41, v192, v41, vcc
	v_cmp_lt_i32_e32 vcc, -1, v139
	s_nop 1
	v_cndmask_b32_e32 v58, v192, v58, vcc
	v_cmp_lt_i32_e32 vcc, 31, v139
	v_add_u32_e32 v139, 8, v200
	s_nop 0
	v_cndmask_b32_e32 v42, v192, v42, vcc
	v_cmp_lt_i32_e32 vcc, -1, v139
	s_nop 1
	v_cndmask_b32_e32 v59, v192, v59, vcc
	v_cmp_lt_i32_e32 vcc, 31, v139
	v_add_u32_e32 v139, 3, v200
	s_nop 0
	v_cndmask_b32_e32 v43, v192, v43, vcc
	v_cmp_lt_i32_e32 vcc, -1, v139
	s_nop 1
	v_cndmask_b32_e32 v60, v192, v60, vcc
	v_cmp_lt_i32_e32 vcc, 31, v139
	v_add_u32_e32 v139, 2, v200
	s_nop 0
	v_cndmask_b32_e32 v44, v192, v44, vcc
	v_cmp_lt_i32_e32 vcc, -1, v139
	s_nop 1
	v_cndmask_b32_e32 v61, v192, v61, vcc
	v_cmp_lt_i32_e32 vcc, 31, v139
	v_add_u32_e32 v139, 1, v200
	s_nop 0
	v_cndmask_b32_e32 v45, v192, v45, vcc
	v_cmp_lt_i32_e32 vcc, -1, v139
	s_nop 1
	v_cndmask_b32_e32 v62, v192, v62, vcc
	v_cmp_lt_i32_e32 vcc, 31, v139
	s_nop 1
	v_cndmask_b32_e32 v46, v192, v46, vcc
	v_cmp_lt_i32_e32 vcc, -1, v200
	s_nop 1
	v_cndmask_b32_e32 v63, v192, v63, vcc
	v_cmp_lt_i32_e32 vcc, 31, v200
	s_nop 1
	v_cndmask_b32_e32 v47, v192, v47, vcc

.LBB0_3032:
	s_andn2_b64 vcc, exec, s[6:7]
	s_andn2_b64 s[6:7], s[30:31], exec
	s_and_b64 s[34:35], s[30:31], exec
	s_or_b64 s[34:35], s[6:7], s[34:35]
	s_cbranch_vccnz .LBB0_3024
	v_add_u32_e32 v32, s56, v199
	v_cvt_f32_i32_e32 v32, v32
	v_add_u32_e32 v160, s36, v165
	s_lshl_b32 s6, 1, s41
	ds_read_b128 v[80:83], v160
	ds_read_b128 v[88:91], v160 offset:512
	ds_read_b128 v[96:99], v160 offset:2048
	ds_read_b128 v[104:107], v160 offset:2560
	v_and_b32_e32 v33, s6, v198
	v_cmp_ne_u32_e32 vcc, 0, v33
	v_fma_f32 v32, v137, v32, -v197
	s_or_b64 vcc, s[0:1], vcc
	v_cndmask_b32_e32 v32, v192, v32, vcc
	v_pk_add_f32 v[48:49], v[136:137], v[32:33] op_sel_hi:[1,0]
	v_pk_add_f32 v[50:51], v[142:143], v[32:33] op_sel_hi:[1,0]
	v_pk_add_f32 v[52:53], v[144:145], v[32:33] op_sel_hi:[1,0]
	v_pk_add_f32 v[54:55], v[146:147], v[32:33] op_sel_hi:[1,0]
	v_pk_add_f32 v[56:57], v[148:149], v[32:33] op_sel_hi:[1,0]
	v_pk_add_f32 v[58:59], v[150:151], v[32:33] op_sel_hi:[1,0]
	v_pk_add_f32 v[60:61], v[152:153], v[32:33] op_sel_hi:[1,0]
	v_pk_add_f32 v[62:63], v[154:155], v[32:33] op_sel_hi:[1,0]
	v_mov_b32_e32 v139, v138
	v_pk_add_f32 v[46:47], v[138:139], v[62:63]
	v_pk_add_f32 v[44:45], v[138:139], v[60:61]
	v_pk_add_f32 v[42:43], v[138:139], v[58:59]
	v_pk_add_f32 v[40:41], v[138:139], v[56:57]
	v_pk_add_f32 v[38:39], v[138:139], v[54:55]
	v_pk_add_f32 v[36:37], v[138:139], v[52:53]
	v_pk_add_f32 v[34:35], v[138:139], v[50:51]
	v_pk_add_f32 v[32:33], v[140:141], v[48:49]
	v_add_u32_e32 v139, s36, v166
	ds_read_b64_tr_b16 v[100:101], v139 offset:24576
	ds_read_b64_tr_b16 v[102:103], v139 offset:25088
	ds_read_b64_tr_b16 v[92:93], v139 offset:25600
	ds_read_b64_tr_b16 v[94:95], v139 offset:26112
	ds_read_b128 v[108:111], v160 offset:4096
	ds_read_b128 v[202:205], v160 offset:4608
	s_waitcnt lgkmcnt(0)
	v_mfma_f32_32x32x16_bf16 v[48:63], v[80:83], v[76:79], v[48:63]
	ds_read_b64_tr_b16 v[84:85], v139 offset:26624
	ds_read_b64_tr_b16 v[86:87], v139 offset:27136
	ds_read_b64_tr_b16 v[80:81], v139 offset:27648
	ds_read_b64_tr_b16 v[82:83], v139 offset:28160
	ds_read_b128 v[206:209], v160 offset:6144
	ds_read_b128 v[210:213], v160 offset:6656
	v_mfma_f32_32x32x16_bf16 v[32:47], v[88:91], v[76:79], v[32:47]
	v_mfma_f32_32x32x16_bf16 v[48:63], v[96:99], v[72:75], v[48:63]
	v_mfma_f32_32x32x16_bf16 v[32:47], v[104:107], v[72:75], v[32:47]
	s_add_i32 s32, s40, 2
	s_cmp_ge_u32 s32, s57
	s_cbranch_scc1 .Lmoba1_a
	s_add_i32 s32, s43, s39
	s_mov_b32 m0, s32
	s_nop 0
	global_load_lds_dwordx4 v[156:157], off
	s_add_i32 m0, s32, 0x6000
	s_nop 0
	global_load_lds_dwordx4 v[158:159], off
.Lmoba1_a:
	v_mfma_f32_32x32x16_bf16 v[48:63], v[108:111], v[68:71], v[48:63]
	v_mfma_f32_32x32x16_bf16 v[32:47], v[202:205], v[68:71], v[32:47]
	s_waitcnt lgkmcnt(0)
	v_mfma_f32_32x32x16_bf16 v[48:63], v[206:209], v[64:67], v[48:63]
	ds_read_b64_tr_b16 v[108:109], v139 offset:28672
	ds_read_b64_tr_b16 v[110:111], v139 offset:29184
	ds_read_b64_tr_b16 v[104:105], v139 offset:29696
	ds_read_b64_tr_b16 v[106:107], v139 offset:30208
	v_mfma_f32_32x32x16_bf16 v[32:47], v[210:213], v[64:67], v[32:47]
	ds_read_b64_tr_b16 v[96:97], v139 offset:30720
	ds_read_b64_tr_b16 v[98:99], v139 offset:31232
	ds_read_b64_tr_b16 v[88:89], v139 offset:31744
	ds_read_b64_tr_b16 v[90:91], v139 offset:32256
	s_add_i32 s6, s56, 63
	s_cmp_gt_u32 s6, s8
	s_cselect_b64 s[6:7], -1, 0
	s_and_b64 s[0:1], s[0:1], s[6:7]
	s_andn2_b64 vcc, exec, s[0:1]
	s_cbranch_vccnz .LBB0_3035
	v_add_u32_e32 v139, 27, v200
	v_cmp_lt_i32_e32 vcc, -1, v139
	s_nop 1
	v_cndmask_b32_e32 v48, v192, v48, vcc
	v_cmp_lt_i32_e32 vcc, 31, v139
	v_add_u32_e32 v139, 26, v200
	s_nop 0
	v_cndmask_b32_e32 v32, v192, v32, vcc
	v_cmp_lt_i32_e32 vcc, -1, v139
	s_nop 1
	v_cndmask_b32_e32 v49, v192, v49, vcc
	v_cmp_lt_i32_e32 vcc, 31, v139
	v_add_u32_e32 v139, 25, v200
	s_nop 0
	v_cndmask_b32_e32 v33, v192, v33, vcc
	v_cmp_lt_i32_e32 vcc, -1, v139
	s_nop 1
	v_cndmask_b32_e32 v50, v192, v50, vcc
	v_cmp_lt_i32_e32 vcc, 31, v139
	v_add_u32_e32 v139, 24, v200
	s_nop 0
	v_cndmask_b32_e32 v34, v192, v34, vcc
	v_cmp_lt_i32_e32 vcc, -1, v139
	s_nop 1
	v_cndmask_b32_e32 v51, v192, v51, vcc
	v_cmp_lt_i32_e32 vcc, 31, v139
	v_add_u32_e32 v139, 19, v200
	s_nop 0
	v_cndmask_b32_e32 v35, v192, v35, vcc
	v_cmp_lt_i32_e32 vcc, -1, v139
	s_nop 1
	v_cndmask_b32_e32 v52, v192, v52, vcc
	v_cmp_lt_i32_e32 vcc, 31, v139
	v_add_u32_e32 v139, 18, v200
	s_nop 0
	v_cndmask_b32_e32 v36, v192, v36, vcc
	v_cmp_lt_i32_e32 vcc, -1, v139
	s_nop 1
	v_cndmask_b32_e32 v53, v192, v53, vcc
	v_cmp_lt_i32_e32 vcc, 31, v139
	v_add_u32_e32 v139, 17, v200
	s_nop 0
	v_cndmask_b32_e32 v37, v192, v37, vcc
	v_cmp_lt_i32_e32 vcc, -1, v139
	s_nop 1
	v_cndmask_b32_e32 v54, v192, v54, vcc
	v_cmp_lt_i32_e32 vcc, 31, v139
	v_add_u32_e32 v139, 16, v200
	s_nop 0
	v_cndmask_b32_e32 v38, v192, v38, vcc
	v_cmp_lt_i32_e32 vcc, -1, v139
	s_nop 1
	v_cndmask_b32_e32 v55, v192, v55, vcc
	v_cmp_lt_i32_e32 vcc, 31, v139
	v_add_u32_e32 v139, 11, v200
	s_nop 0
	v_cndmask_b32_e32 v39, v192, v39, vcc
	v_cmp_lt_i32_e32 vcc, -1, v139
	s_nop 1
	v_cndmask_b32_e32 v56, v192, v56, vcc
	v_cmp_lt_i32_e32 vcc, 31, v139
	v_add_u32_e32 v139, 10, v200
	s_nop 0
	v_cndmask_b32_e32 v40, v192, v40, vcc
	v_cmp_lt_i32_e32 vcc, -1, v139
	s_nop 1
	v_cndmask_b32_e32 v57, v192, v57, vcc
	v_cmp_lt_i32_e32 vcc, 31, v139
	v_add_u32_e32 v139, 9, v200
	s_nop 0
	v_cndmask_b32_e32 v41, v192, v41, vcc
	v_cmp_lt_i32_e32 vcc, -1, v139
	s_nop 1
	v_cndmask_b32_e32 v58, v192, v58, vcc
	v_cmp_lt_i32_e32 vcc, 31, v139
	v_add_u32_e32 v139, 8, v200
	s_nop 0
	v_cndmask_b32_e32 v42, v192, v42, vcc
	v_cmp_lt_i32_e32 vcc, -1, v139
	s_nop 1
	v_cndmask_b32_e32 v59, v192, v59, vcc
	v_cmp_lt_i32_e32 vcc, 31, v139
	v_add_u32_e32 v139, 3, v200
	s_nop 0
	v_cndmask_b32_e32 v43, v192, v43, vcc
	v_cmp_lt_i32_e32 vcc, -1, v139
	s_nop 1
	v_cndmask_b32_e32 v60, v192, v60, vcc
	v_cmp_lt_i32_e32 vcc, 31, v139
	v_add_u32_e32 v139, 2, v200
	s_nop 0
	v_cndmask_b32_e32 v44, v192, v44, vcc
	v_cmp_lt_i32_e32 vcc, -1, v139
	s_nop 1
	v_cndmask_b32_e32 v61, v192, v61, vcc
	v_cmp_lt_i32_e32 vcc, 31, v139
	v_add_u32_e32 v139, 1, v200
	s_nop 0
	v_cndmask_b32_e32 v45, v192, v45, vcc
	v_cmp_lt_i32_e32 vcc, -1, v139
	s_nop 1
	v_cndmask_b32_e32 v62, v192, v62, vcc
	v_cmp_lt_i32_e32 vcc, 31, v139
	s_nop 1
	v_cndmask_b32_e32 v46, v192, v46, vcc
	v_cmp_lt_i32_e32 vcc, -1, v200
	s_nop 1
	v_cndmask_b32_e32 v63, v192, v63, vcc
	v_cmp_lt_i32_e32 vcc, 31, v200
	s_nop 1
	v_cndmask_b32_e32 v47, v192, v47, vcc
